# scan loop: LDS fragment reads in half batches issued as soon as their registers free up, counted lgkmcnt waits at first use
# baseline (speedup 1.0000x reference)
; DI float bflo(unsigned u) { return __uint_as_float(u << 16); }
; DI float bfhi(unsigned u) { return __uint_as_float(u & 0xffff0000u); }
; DI bf16x8 packS(const f32x16& x, int s) { return pack8(x[8 * s], x[8 * s + 1], x[8 * s + 2], x[8 * s + 3], x[8 * s + 4], x[8 * s + 5], x[8 * s + 6], x[8 * s + 7]); }
; #define SCAN_RDW(F, mh) do { _Pragma("unroll") for (int k = 0; k < 8; ++k) { const int i2 = k >> 2, m = 2 * (mh) + ((k >> 1) & 1), sx = k & 1; F[k] = *(const bf16x8*)(lw + ((i2 * 4 + m) * 2 + sx) * 1024); } } while (0)
; DI void gdn_scan_seq(const Params& p, int bh16, char* ldsf) {
;     ...
;     for (int m = 0; m < 4; ++m) { Sb[m][0] = packS(S[m], 0); Sb[m][1] = packS(S[m], 1); *(bf16x8*)(sco + (m * 2 + 0) * 1024) = Sb[m][0]; *(bf16x8*)(sco + (m * 2 + 1) * 1024) = Sb[m][1]; }
;     __builtin_amdgcn_sched_barrier(0);
;     if (c + 2 < 128) { const int s2 = sl >= 1 ? sl - 1 : 2; SCAN_ISSUE(c + 2, s2); }
;     const char* base = ldsf + sl * 49152;
;     const char* lw = base + lane * 16; const char* lk = lw + 16384; const char* lu = base + 32768 + wv * 4096 + lane * 16;
;     const float gl = glt[c];
;     f32x16 vn[2];
; #pragma unroll
;     for (int i2 = 0; i2 < 2; ++i2) {
;       const u32x4 ua = *(const u32x4*)(lu + (2 * i2) * 1024), ub = *(const u32x4*)(lu + (2 * i2 + 1) * 1024);
; #pragma unroll
;       for (int e = 0; e < 4; ++e) { vn[i2][2 * e] = bflo(ua[e]); vn[i2][2 * e + 1] = bfhi(ua[e]); vn[i2][8 + 2 * e] = bflo(ub[e]); vn[i2][8 + 2 * e + 1] = bfhi(ub[e]); }
;     }
;     bf16x8 fa[8], fb[8];
;     ...
;     SCAN_RDW(fa, 0);
;     __builtin_amdgcn_sched_barrier(0);
;     SCAN_RDW(fb, 1);
;     __builtin_amdgcn_sched_barrier(0);
;     SCAN_MMW(fa, 0);
;     __builtin_amdgcn_sched_barrier(0);
;     SCAN_RDK(fa, 0);
;     __builtin_amdgcn_sched_barrier(0);
;     SCAN_MMW(fb, 1);
;     __builtin_amdgcn_sched_barrier(0);
;     SCAN_RDK(fb, 1);
;     __builtin_amdgcn_sched_barrier(0);
;     bf16x8 Vb[2][2];
; #pragma unroll
;     for (int j2 = 0; j2 < 2; ++j2) { Vb[j2][0] = packS(vn[j2], 0); Vb[j2][1] = packS(vn[j2], 1); }
; #pragma unroll
;     for (int m = 0; m < 4; ++m)
; #pragma unroll
;       for (int r = 0; r < 16; ++r) S[m][r] *= gl;
;     SCAN_MMK(fa, 0);
.Lscan_noprog:
	v_add_u32_e32 v131, s3, v130
	v_add_u32_e32 v134, s3, v129
	v_mov_b32_e32 v143, s18
	ds_read_b128 v[72:75], v134 offset:32768
	ds_read_b128 v[76:79], v134 offset:33792
	ds_read_b32 v142, v143
	ds_read_b128 v[148:151], v131 offset:0
	ds_read_b128 v[152:155], v131 offset:1024
	ds_read_b128 v[156:159], v131 offset:2048
	ds_read_b128 v[160:163], v131 offset:3072
	ds_read_b128 v[164:167], v131 offset:4096
	ds_read_b128 v[168:171], v131 offset:5120
	ds_read_b128 v[172:175], v131 offset:6144
	ds_read_b128 v[178:181], v131 offset:7168
	ds_read_b128 v[88:91], v134 offset:34816
	ds_read_b128 v[92:95], v134 offset:35840
	s_waitcnt lgkmcnt(10)
	v_mfma_f32_32x32x16_bf16 v[0:15], v[182:185], v[80:83], v[0:15]
	v_lshlrev_b32_e32 v64, 16, v72
	v_and_b32_e32 v65, 0xffff0000, v72
	v_lshlrev_b32_e32 v66, 16, v73
	v_and_b32_e32 v67, 0xffff0000, v73
	v_mfma_f32_32x32x16_bf16 v[0:15], v[190:193], v[84:87], v[0:15]
	v_lshlrev_b32_e32 v68, 16, v74
	v_and_b32_e32 v69, 0xffff0000, v74
	v_lshlrev_b32_e32 v70, 16, v75
	v_and_b32_e32 v71, 0xffff0000, v75
	v_mfma_f32_32x32x16_bf16 v[16:31], v[194:197], v[80:83], v[16:31]
	v_lshlrev_b32_e32 v72, 16, v76
	v_and_b32_e32 v73, 0xffff0000, v76
	v_lshlrev_b32_e32 v74, 16, v77
	v_and_b32_e32 v75, 0xffff0000, v77
	v_mfma_f32_32x32x16_bf16 v[16:31], v[198:201], v[84:87], v[16:31]
	v_lshlrev_b32_e32 v76, 16, v78
	v_and_b32_e32 v77, 0xffff0000, v78
	v_lshlrev_b32_e32 v78, 16, v79
	v_and_b32_e32 v79, 0xffff0000, v79
	s_waitcnt lgkmcnt(8)
	ds_read_b128 v[182:185], v131 offset:8192
	ds_read_b128 v[190:193], v131 offset:9216
	ds_read_b128 v[194:197], v131 offset:10240
	ds_read_b128 v[198:201], v131 offset:11264
	v_mfma_f32_32x32x16_bf16 v[32:47], v[202:205], v[80:83], v[32:47]
	v_cvt_pk_bf16_f32 v96, v0, v1
	v_cvt_pk_bf16_f32 v97, v2, v3
	v_cvt_pk_bf16_f32 v98, v4, v5
	v_cvt_pk_bf16_f32 v99, v6, v7
	v_cvt_pk_bf16_f32 v100, v8, v9
	v_mfma_f32_32x32x16_bf16 v[32:47], v[208:211], v[84:87], v[32:47]
	v_cvt_pk_bf16_f32 v101, v10, v11
	v_cvt_pk_bf16_f32 v102, v12, v13
	v_cvt_pk_bf16_f32 v103, v14, v15
	v_mfma_f32_32x32x16_bf16 v[48:63], v[212:215], v[80:83], v[48:63]
	v_cvt_pk_bf16_f32 v104, v16, v17
	v_cvt_pk_bf16_f32 v105, v18, v19
	v_cvt_pk_bf16_f32 v106, v20, v21
	v_cvt_pk_bf16_f32 v107, v22, v23
	v_cvt_pk_bf16_f32 v108, v24, v25
	v_mfma_f32_32x32x16_bf16 v[48:63], v[216:219], v[84:87], v[48:63]
	v_cvt_pk_bf16_f32 v109, v26, v27
	v_cvt_pk_bf16_f32 v110, v28, v29
	v_cvt_pk_bf16_f32 v111, v30, v31
	s_waitcnt lgkmcnt(4)
	ds_read_b128 v[202:205], v131 offset:12288
	ds_read_b128 v[208:211], v131 offset:13312
	ds_read_b128 v[212:215], v131 offset:14336
	ds_read_b128 v[216:219], v131 offset:15360
	v_mfma_f32_32x32x16_bf16 v[64:79], v[148:151], v[96:99], v[64:79]
	v_cvt_pk_bf16_f32 v112, v32, v33
	v_cvt_pk_bf16_f32 v113, v34, v35
	v_cvt_pk_bf16_f32 v114, v36, v37
	v_cvt_pk_bf16_f32 v115, v38, v39
	v_lshlrev_b32_e32 v80, 16, v88
	v_mfma_f32_32x32x16_bf16 v[64:79], v[152:155], v[100:103], v[64:79]
	v_cvt_pk_bf16_f32 v116, v40, v41
	v_cvt_pk_bf16_f32 v117, v42, v43
	v_cvt_pk_bf16_f32 v118, v44, v45
	v_cvt_pk_bf16_f32 v119, v46, v47
	v_and_b32_e32 v81, 0xffff0000, v88
	v_mfma_f32_32x32x16_bf16 v[64:79], v[156:159], v[104:107], v[64:79]
	v_cvt_pk_bf16_f32 v120, v48, v49
	v_cvt_pk_bf16_f32 v121, v50, v51
	v_cvt_pk_bf16_f32 v122, v52, v53
	v_cvt_pk_bf16_f32 v123, v54, v55
	v_lshlrev_b32_e32 v82, 16, v89
	v_mfma_f32_32x32x16_bf16 v[64:79], v[160:163], v[108:111], v[64:79]
	v_cvt_pk_bf16_f32 v124, v56, v57
	v_cvt_pk_bf16_f32 v125, v58, v59
	v_cvt_pk_bf16_f32 v126, v60, v61
	v_cvt_pk_bf16_f32 v127, v62, v63
	v_and_b32_e32 v83, 0xffff0000, v89
	ds_read_b128 v[148:151], v131 offset:16384
	ds_read_b128 v[152:155], v131 offset:17408
	ds_read_b128 v[156:159], v131 offset:20480
	ds_read_b128 v[160:163], v131 offset:21504
	v_mfma_f32_32x32x16_bf16 v[64:79], v[164:167], v[112:115], v[64:79]
	v_lshlrev_b32_e32 v84, 16, v90
	v_and_b32_e32 v85, 0xffff0000, v90
	v_lshlrev_b32_e32 v86, 16, v91
	v_and_b32_e32 v87, 0xffff0000, v91
	v_lshlrev_b32_e32 v88, 16, v92
	global_store_dwordx4 v128, v[96:99], s[8:9]
	v_mfma_f32_32x32x16_bf16 v[64:79], v[168:171], v[116:119], v[64:79]
	v_and_b32_e32 v89, 0xffff0000, v92
	v_lshlrev_b32_e32 v90, 16, v93
	v_and_b32_e32 v91, 0xffff0000, v93
	v_lshlrev_b32_e32 v92, 16, v94
	v_and_b32_e32 v93, 0xffff0000, v94
	global_store_dwordx4 v128, v[100:103], s[8:9] offset:1024
	v_mfma_f32_32x32x16_bf16 v[64:79], v[172:175], v[120:123], v[64:79]
	v_lshlrev_b32_e32 v94, 16, v95
	v_and_b32_e32 v95, 0xffff0000, v95
	global_store_dwordx4 v128, v[104:107], s[8:9] offset:2048
	global_store_dwordx4 v128, v[108:111], s[8:9] offset:3072
	v_mul_f32_e32 v0, v142, v0
	v_mfma_f32_32x32x16_bf16 v[64:79], v[178:181], v[124:127], v[64:79]
	v_mul_f32_e32 v1, v142, v1
	v_mul_f32_e32 v2, v142, v2
	v_mul_f32_e32 v3, v142, v3
	v_mul_f32_e32 v4, v142, v4
	v_mul_f32_e32 v5, v142, v5
	s_waitcnt lgkmcnt(8)
; DI bf16x8 packS(const f32x16& x, int s) { return pack8(x[8 * s], x[8 * s + 1], x[8 * s + 2], x[8 * s + 3], x[8 * s + 4], x[8 * s + 5], x[8 * s + 6], x[8 * s + 7]); }
; #define SCAN_MMK(F, mh) do { _Pragma("unroll") for (int q = 0; q < 4; ++q) { const int j2 = q >> 1, sx = q & 1; S[2 * (mh)] = MFMA32(F[q], Vb[j2][sx], S[2 * (mh)]); S[2 * (mh) + 1] = MFMA32(F[4 + q], Vb[j2][sx], S[2 * (mh) + 1]); } } while (0)
; DI void gdn_scan_seq(const Params& p, int bh16, char* ldsf) {
;     ...
;     bf16x8 Vb[2][2];
; #pragma unroll
;     for (int j2 = 0; j2 < 2; ++j2) { Vb[j2][0] = packS(vn[j2], 0); Vb[j2][1] = packS(vn[j2], 1); }
; #pragma unroll
;     for (int m = 0; m < 4; ++m)
; #pragma unroll
;       for (int r = 0; r < 16; ++r) S[m][r] *= gl;
;     SCAN_MMK(fa, 0);
;     SCAN_MMK(fb, 1);
;     ...
;     asm volatile("s_waitcnt lgkmcnt(0)" ::: "memory");
;     sl = sl == 2 ? 0 : sl + 1;
;   }
	ds_read_b128 v[164:167], v131 offset:24576
	ds_read_b128 v[168:171], v131 offset:25600
	ds_read_b128 v[172:175], v131 offset:28672
	ds_read_b128 v[178:181], v131 offset:29696
	v_mfma_f32_32x32x16_bf16 v[80:95], v[182:185], v[96:99], v[80:95]
	v_mul_f32_e32 v6, v142, v6
	v_mul_f32_e32 v7, v142, v7
	v_mul_f32_e32 v8, v142, v8
	v_mul_f32_e32 v9, v142, v9
	v_mul_f32_e32 v10, v142, v10
	v_mfma_f32_32x32x16_bf16 v[80:95], v[190:193], v[100:103], v[80:95]
	v_mul_f32_e32 v11, v142, v11
	v_mul_f32_e32 v12, v142, v12
	v_mul_f32_e32 v13, v142, v13
	v_mul_f32_e32 v14, v142, v14
	v_mul_f32_e32 v15, v142, v15
	v_mfma_f32_32x32x16_bf16 v[80:95], v[194:197], v[104:107], v[80:95]
	v_mul_f32_e32 v16, v142, v16
	v_mul_f32_e32 v17, v142, v17
	v_mul_f32_e32 v18, v142, v18
	v_mul_f32_e32 v19, v142, v19
	global_store_dwordx4 v128, v[112:115], s[10:11]
	v_mul_f32_e32 v32, v142, v32
	v_mfma_f32_32x32x16_bf16 v[80:95], v[198:201], v[108:111], v[80:95]
	v_mul_f32_e32 v20, v142, v20
	v_mul_f32_e32 v21, v142, v21
	v_mul_f32_e32 v22, v142, v22
	v_mul_f32_e32 v23, v142, v23
	global_store_dwordx4 v128, v[116:119], s[10:11] offset:1024
	v_mul_f32_e32 v33, v142, v33
	s_waitcnt lgkmcnt(8)
	ds_read_b128 v[182:185], v131 offset:18432
	ds_read_b128 v[190:193], v131 offset:19456
	ds_read_b128 v[194:197], v131 offset:22528
	ds_read_b128 v[198:201], v131 offset:23552
	v_mfma_f32_32x32x16_bf16 v[80:95], v[202:205], v[112:115], v[80:95]
	v_mul_f32_e32 v24, v142, v24
	v_mul_f32_e32 v25, v142, v25
	v_mul_f32_e32 v26, v142, v26
	v_mul_f32_e32 v27, v142, v27
	global_store_dwordx4 v128, v[120:123], s[10:11] offset:2048
	v_mul_f32_e32 v34, v142, v34
	v_mfma_f32_32x32x16_bf16 v[80:95], v[208:211], v[116:119], v[80:95]
	v_mul_f32_e32 v28, v142, v28
	v_mul_f32_e32 v29, v142, v29
	v_mul_f32_e32 v30, v142, v30
	v_mul_f32_e32 v31, v142, v31
	global_store_dwordx4 v128, v[124:127], s[10:11] offset:3072
	v_mul_f32_e32 v35, v142, v35
	v_mfma_f32_32x32x16_bf16 v[80:95], v[212:215], v[120:123], v[80:95]
	v_cvt_pk_bf16_f32 v64, v64, v65
	v_cvt_pk_bf16_f32 v65, v66, v67
	v_cvt_pk_bf16_f32 v66, v68, v69
	v_cvt_pk_bf16_f32 v67, v70, v71
	v_cvt_pk_bf16_f32 v68, v72, v73
	v_mul_f32_e32 v36, v142, v36
	v_mfma_f32_32x32x16_bf16 v[80:95], v[216:219], v[124:127], v[80:95]
	v_cvt_pk_bf16_f32 v69, v74, v75
	v_cvt_pk_bf16_f32 v70, v76, v77
	v_cvt_pk_bf16_f32 v71, v78, v79
	v_mul_f32_e32 v37, v142, v37
	v_mul_f32_e32 v38, v142, v38
	v_mul_f32_e32 v39, v142, v39
	s_waitcnt lgkmcnt(8)
	ds_read_b128 v[202:205], v131 offset:26624
	ds_read_b128 v[208:211], v131 offset:27648
	ds_read_b128 v[212:215], v131 offset:30720
	ds_read_b128 v[216:219], v131 offset:31744
	v_mfma_f32_32x32x16_bf16 v[0:15], v[148:151], v[64:67], v[0:15]
	v_mul_f32_e32 v40, v142, v40
	v_mul_f32_e32 v41, v142, v41
	v_mul_f32_e32 v42, v142, v42
	v_mul_f32_e32 v43, v142, v43
	v_mul_f32_e32 v44, v142, v44
	v_mul_f32_e32 v45, v142, v45
	s_add_u32 s2, s2, 1
	s_add_u32 s3, s3, 0xc000
	s_cmp_eq_u32 s3, 0x24000
	s_cselect_b32 s3, 0, s3
	s_add_u32 s18, s18, 4
	s_add_u32 s8, s8, 0x8000
	s_addc_u32 s9, s9, 0
	s_add_u32 s10, s10, 0x8000
	s_addc_u32 s11, s11, 0
	v_mfma_f32_32x32x16_bf16 v[0:15], v[152:155], v[68:71], v[0:15]
	v_mul_f32_e32 v46, v142, v46
	v_mul_f32_e32 v47, v142, v47
	v_mul_f32_e32 v48, v142, v48
	v_mul_f32_e32 v49, v142, v49
	v_mul_f32_e32 v50, v142, v50
	v_mul_f32_e32 v51, v142, v51
	v_mfma_f32_32x32x16_bf16 v[16:31], v[156:159], v[64:67], v[16:31]
	v_mul_f32_e32 v52, v142, v52
	v_mul_f32_e32 v53, v142, v53
	v_mul_f32_e32 v54, v142, v54
	v_mul_f32_e32 v55, v142, v55
	v_mul_f32_e32 v56, v142, v56
	v_mul_f32_e32 v57, v142, v57
	v_mfma_f32_32x32x16_bf16 v[16:31], v[160:163], v[68:71], v[16:31]
	v_mul_f32_e32 v58, v142, v58
	v_mul_f32_e32 v59, v142, v59
	v_mul_f32_e32 v60, v142, v60
	v_mul_f32_e32 v61, v142, v61
	v_mul_f32_e32 v62, v142, v62
	v_mul_f32_e32 v63, v142, v63
	s_waitcnt lgkmcnt(8)
	v_mfma_f32_32x32x16_bf16 v[32:47], v[164:167], v[64:67], v[32:47]
	v_cvt_pk_bf16_f32 v80, v80, v81
	v_cvt_pk_bf16_f32 v81, v82, v83
	v_cvt_pk_bf16_f32 v82, v84, v85
	v_cvt_pk_bf16_f32 v83, v86, v87
	v_cvt_pk_bf16_f32 v84, v88, v89
	v_cvt_pk_bf16_f32 v85, v90, v91
	v_mfma_f32_32x32x16_bf16 v[32:47], v[168:171], v[68:71], v[32:47]
	v_cvt_pk_bf16_f32 v86, v92, v93
	v_cvt_pk_bf16_f32 v87, v94, v95
	v_mfma_f32_32x32x16_bf16 v[48:63], v[172:175], v[64:67], v[48:63]
	v_mfma_f32_32x32x16_bf16 v[48:63], v[178:181], v[68:71], v[48:63]
	s_cmp_lt_u32 s2, 0x80
	s_waitcnt lgkmcnt(0)
	s_cbranch_scc1 .Lscan_loop
	s_waitcnt vmcnt(0)
	s_barrier
